# v10 plus HGRN: redundant chunk-top barrier removed; mixers queue pop: no all-wave vmcnt(0) drain between the pop barriers
# speedup vs baseline: 1.0043x; 1.0006x over previous
.LBB0_528:
	s_or_b64 exec, exec, s[4:5]
	v_mov_b32_e32 v0, s26
	s_waitcnt lgkmcnt(0)
	s_barrier
	ds_read_b32 v0, v0
	s_mov_b64 s[4:5], -1
	s_waitcnt lgkmcnt(0)
	v_cmp_le_i32_e32 vcc, s90, v0
	v_readfirstlane_b32 s1, v0
	s_cbranch_vccnz .LBB0_523
	v_mov_b32_e32 v146, v235
	v_cmp_eq_u32_e32 vcc, 0, v146
	s_and_saveexec_b64 s[6:7], vcc
	s_cbranch_execz .Lmy_q1
	v_mov_b32_e32 v253, 1
	global_atomic_add v253, v48, v253, s[92:93] sc0

.LBB0_894:
	v_lshlrev_b32_e32 v208, 16, v77
	v_add_f32_e32 v195, 0, v208
	v_lshlrev_b32_e32 v207, 16, v61
	v_add_f32_e32 v194, v195, v207
	v_lshlrev_b32_e32 v206, 16, v63
	v_add_f32_e32 v193, v194, v206
	v_lshlrev_b32_e32 v91, 16, v65
	v_add_f32_e32 v103, v193, v91
	v_lshlrev_b32_e32 v205, 16, v67
	v_add_f32_e32 v104, v103, v205
	v_lshlrev_b32_e32 v204, 16, v69
	v_add_f32_e32 v106, v104, v204
	v_lshlrev_b32_e32 v203, 16, v71
	v_add_f32_e32 v105, v106, v203
	v_lshlrev_b32_e32 v202, 16, v73
	v_add_f32_e32 v107, v105, v202
	v_lshlrev_b32_e32 v201, 16, v75
	v_add_f32_e32 v108, v107, v201
	v_lshlrev_b32_e32 v47, 16, v83
	v_add_f32_e32 v192, v108, v47
	v_lshlrev_b32_e32 v46, 16, v89
	v_add_f32_e32 v109, v192, v46
	v_lshlrev_b32_e32 v200, 16, v124
	v_add_f32_e32 v191, v109, v200
	v_lshlrev_b32_e32 v199, 16, v130
	v_add_f32_e32 v190, v191, v199
	v_lshlrev_b32_e32 v198, 16, v137
	v_add_f32_e32 v189, v190, v198
	v_lshlrev_b32_e32 v197, 16, v138
	v_add_f32_e32 v49, v189, v197
	v_lshlrev_b32_e32 v196, 16, v142
	v_add_f32_e32 v41, v49, v196
	v_mul_f32_e32 v40, 0x3fb8aa3b, v41
	v_exp_f32_e32 v40, v40
	s_add_i32 s1, s8, 1
	s_cmp_eq_u32 s8, 31
	s_waitcnt vmcnt(1)
	ds_write_b128 v131, v[32:35] offset:53248
	s_waitcnt vmcnt(0)
	ds_write_b128 v131, v[36:39] offset:61952
	ds_write_b32 v132, v40
	s_cbranch_scc1 .LBB0_896
	s_mul_i32 s26, s1, 0x48000
	s_lshl_b64 s[4:5], s[26:27], 1
	v_lshl_add_u64 v[32:33], v[50:51], 0, s[4:5]
	v_add_co_u32_e32 v34, vcc, 0x2000, v32
	global_load_ushort v139, v[32:33], off
	global_load_ushort v77, v[32:33], off offset:1024
	v_addc_co_u32_e32 v35, vcc, 0, v33, vcc
	global_load_ushort v140, v[34:35], off offset:1024
	global_load_ushort v61, v[34:35], off offset:2048
	v_add_co_u32_e32 v34, vcc, 0x4000, v32
	s_mov_b32 s6, 0x21000
	s_nop 0
	v_addc_co_u32_e32 v35, vcc, 0, v33, vcc
	global_load_ushort v141, v[34:35], off offset:2048
	global_load_ushort v63, v[34:35], off offset:3072
	v_add_co_u32_e32 v34, vcc, 0x6000, v32
	v_lshl_add_u64 v[36:37], v[56:57], 0, s[4:5]
	s_nop 0
	v_addc_co_u32_e32 v35, vcc, 0, v33, vcc
	global_load_ushort v143, v[34:35], off offset:3072
	v_add_co_u32_e32 v34, vcc, 0x7000, v32
	s_nop 1
	v_addc_co_u32_e32 v35, vcc, 0, v33, vcc
	global_load_ushort v65, v[34:35], off
	v_add_co_u32_e32 v34, vcc, 0x9000, v32
	s_nop 1
	v_addc_co_u32_e32 v35, vcc, 0, v33, vcc
	global_load_ushort v144, v[34:35], off
	global_load_ushort v67, v[34:35], off offset:1024
	v_add_co_u32_e32 v34, vcc, 0xb000, v32
	s_nop 1
	v_addc_co_u32_e32 v35, vcc, 0, v33, vcc
	global_load_ushort v145, v[34:35], off offset:1024
	global_load_ushort v69, v[34:35], off offset:2048
	v_add_co_u32_e32 v34, vcc, 0xd000, v32
	s_nop 1
	v_addc_co_u32_e32 v35, vcc, 0, v33, vcc
	global_load_ushort v147, v[34:35], off offset:2048
	global_load_ushort v71, v[34:35], off offset:3072
	v_add_co_u32_e32 v34, vcc, 0xf000, v32
	s_nop 1
	v_addc_co_u32_e32 v35, vcc, 0, v33, vcc
	global_load_ushort v148, v[34:35], off offset:3072
	v_add_co_u32_e32 v34, vcc, s31, v32
	s_nop 1
	v_addc_co_u32_e32 v35, vcc, 0, v33, vcc
	global_load_ushort v73, v[34:35], off
	v_add_co_u32_e32 v34, vcc, s33, v32
	s_nop 1
	v_addc_co_u32_e32 v35, vcc, 0, v33, vcc
	global_load_ushort v149, v[34:35], off
	global_load_ushort v75, v[34:35], off offset:1024
	v_add_co_u32_e32 v34, vcc, s23, v32
	s_nop 1
	v_addc_co_u32_e32 v35, vcc, 0, v33, vcc
	global_load_ushort v150, v[34:35], off offset:1024
	global_load_ushort v83, v[34:35], off offset:2048
	v_add_co_u32_e32 v34, vcc, s81, v32
	s_nop 1
	v_addc_co_u32_e32 v35, vcc, 0, v33, vcc
	global_load_ushort v151, v[34:35], off offset:2048
	global_load_ushort v89, v[34:35], off offset:3072
	v_add_co_u32_e32 v34, vcc, s11, v32
	s_nop 1
	v_addc_co_u32_e32 v35, vcc, 0, v33, vcc
	global_load_ushort v152, v[34:35], off offset:3072
	v_add_co_u32_e32 v34, vcc, s68, v32
	s_nop 1
	v_addc_co_u32_e32 v35, vcc, 0, v33, vcc
	global_load_ushort v124, v[34:35], off
	v_add_co_u32_e32 v34, vcc, s72, v32
	s_nop 1
	v_addc_co_u32_e32 v35, vcc, 0, v33, vcc
	global_load_ushort v153, v[34:35], off
	global_load_ushort v130, v[34:35], off offset:1024
	v_add_co_u32_e32 v34, vcc, s71, v32
	s_nop 1
	v_addc_co_u32_e32 v35, vcc, 0, v33, vcc
	global_load_ushort v154, v[34:35], off offset:1024
	global_load_ushort v137, v[34:35], off offset:2048
	v_add_co_u32_e32 v34, vcc, s70, v32
	s_nop 1
	v_addc_co_u32_e32 v35, vcc, 0, v33, vcc
	global_load_ushort v155, v[34:35], off offset:2048
	global_load_ushort v138, v[34:35], off offset:3072
	v_add_co_u32_e32 v34, vcc, s6, v32
	s_movk_i32 s6, 0x5000
	s_nop 0
	v_addc_co_u32_e32 v35, vcc, 0, v33, vcc
	v_add_co_u32_e32 v32, vcc, s69, v32
	global_load_ushort v156, v[34:35], off offset:3072
	s_nop 0
	v_addc_co_u32_e32 v33, vcc, 0, v33, vcc
	global_load_ushort v142, v[32:33], off
	v_lshl_add_u64 v[32:33], v[54:55], 0, s[4:5]
	v_add_co_u32_e32 v34, vcc, s7, v32
	global_load_ushort v157, v[32:33], off offset:3072
	s_nop 0
	v_addc_co_u32_e32 v35, vcc, 0, v33, vcc
	global_load_ushort v158, v[34:35], off
	v_add_co_u32_e32 v34, vcc, s6, v32
	s_mov_b32 s6, 0x24000
	s_nop 0
	v_addc_co_u32_e32 v35, vcc, 0, v33, vcc
	global_load_ushort v159, v[34:35], off offset:1024
	v_add_co_u32_e32 v34, vcc, s0, v32
	s_nop 1
	v_addc_co_u32_e32 v35, vcc, 0, v33, vcc
	global_load_ushort v160, v[34:35], off offset:2048
	v_add_co_u32_e32 v34, vcc, s6, v32
	s_mov_b32 s6, 0x27000
	s_nop 0
	v_addc_co_u32_e32 v35, vcc, 0, v33, vcc
	global_load_ushort v161, v[34:35], off offset:3072
	v_add_co_u32_e32 v34, vcc, s6, v32
	s_mov_b32 s6, 0x29000
	s_nop 0
	v_addc_co_u32_e32 v35, vcc, 0, v33, vcc
	global_load_ushort v162, v[34:35], off
	v_add_co_u32_e32 v34, vcc, s6, v32
	s_mov_b32 s6, 0x2b000
	s_nop 0
	v_addc_co_u32_e32 v35, vcc, 0, v33, vcc
	global_load_ushort v163, v[34:35], off offset:1024
	v_add_co_u32_e32 v34, vcc, s6, v32
	s_mov_b32 s6, 0x4b000
	s_nop 0
	v_addc_co_u32_e32 v35, vcc, 0, v33, vcc
	global_load_ushort v164, v[34:35], off offset:2048
	v_add_co_u32_e32 v34, vcc, s73, v32
	s_nop 1
	v_addc_co_u32_e32 v35, vcc, 0, v33, vcc
	global_load_ushort v165, v[34:35], off offset:3072
	v_add_co_u32_e32 v34, vcc, s6, v32
	s_mov_b32 s6, 0x4d000
	s_nop 0
	v_addc_co_u32_e32 v35, vcc, 0, v33, vcc
	global_load_ushort v166, v[34:35], off
	v_add_co_u32_e32 v34, vcc, s6, v32
	s_mov_b32 s6, 0x4f000
	s_nop 0
	v_addc_co_u32_e32 v35, vcc, 0, v33, vcc
	global_load_ushort v167, v[34:35], off offset:1024
	v_add_co_u32_e32 v34, vcc, s6, v32
	s_mov_b32 s6, 0x6c000
	s_nop 0
	v_addc_co_u32_e32 v35, vcc, 0, v33, vcc
	global_load_ushort v168, v[34:35], off offset:2048
	v_add_co_u32_e32 v34, vcc, s6, v32
	s_nop 1
	v_addc_co_u32_e32 v35, vcc, 0, v33, vcc
	global_load_ushort v169, v[34:35], off offset:3072
	v_add_co_u32_e32 v34, vcc, 0x6f000, v32
	s_nop 1
	v_addc_co_u32_e32 v35, vcc, 0, v33, vcc
	global_load_ushort v170, v[34:35], off
	v_add_co_u32_e32 v34, vcc, 0x71000, v32
	s_nop 1
	v_addc_co_u32_e32 v35, vcc, 0, v33, vcc
	v_add_co_u32_e32 v32, vcc, 0x73000, v32
	global_load_ushort v171, v[34:35], off offset:1024
	s_nop 0
	v_addc_co_u32_e32 v33, vcc, 0, v33, vcc
	global_load_ushort v172, v[32:33], off offset:2048
	s_nop 0
	global_load_dwordx4 v[32:35], v[36:37], off offset:2048
	v_add_co_u32_e32 v36, vcc, 0x48000, v36
	s_nop 1
	v_addc_co_u32_e32 v37, vcc, 0, v37, vcc
	global_load_dwordx4 v[36:39], v[36:37], off offset:2048
